# phase-0 rmsnorm loop: norm weights preloaded once before the row loop (8 per-row reloads and their vmcnt(0) waits removed), on top of the kpe / epilogue de-serialisation version
# speedup vs baseline: 1.0046x; 1.0046x over previous
.LBB0_173:
	s_cmpk_gt_i32 s96, 0x3fff
	s_cbranch_scc1 .LBB0_192
	v_mov_b32_e32 v3, 0
	v_readlane_b32 s36, v236, 35
	v_lshlrev_b32_e32 v4, 4, v78
	v_mov_b32_e32 v5, v3
	v_readlane_b32 s40, v236, 39
	v_readlane_b32 s41, v236, 40
	v_readlane_b32 s42, v236, 41
	v_readlane_b32 s43, v236, 42
	v_readlane_b32 s44, v236, 43
	v_readlane_b32 s45, v236, 44
	v_readlane_b32 s46, v236, 45
	v_readlane_b32 s47, v236, 46
	v_lshl_add_u64 v[30:31], s[42:43], 0, v[4:5]
	v_readlane_b32 s40, v237, 21
	v_readlane_b32 s41, v237, 22
	s_mov_b64 s[6:7], 0x1400
	s_cmp_lg_u64 s[40:41], 0
	v_lshl_add_u64 v[34:35], v[30:31], 0, s[6:7]
	s_mov_b64 s[6:7], 0x1800
	s_cselect_b64 s[0:1], -1, 0
	v_lshl_add_u64 v[36:37], v[30:31], 0, s[6:7]
	s_mov_b64 s[6:7], 0x1c00
	s_ashr_i32 s97, s96, 31
	v_lshl_add_u64 v[38:39], v[30:31], 0, s[6:7]
	s_lshl_b64 s[6:7], s[96:97], 13
	v_readlane_b32 s37, v236, 36
	s_add_u32 s6, s36, s6
	s_addc_u32 s7, s37, s7
	s_mov_b64 s[2:3], 0x1000
	v_lshl_add_u64 v[4:5], s[6:7], 0, v[4:5]
	s_ashr_i32 s93, s92, 31
	v_lshl_add_u64 v[32:33], v[30:31], 0, s[2:3]
	v_lshl_add_u64 v[40:41], v[4:5], 0, s[2:3]
	s_lshl_b64 s[2:3], s[92:93], 13
	s_lshl_b64 s[6:7], s[96:97], 11
	s_add_u32 s6, s40, s6
	v_lshlrev_b32_e32 v2, 2, v78
	v_readlane_b32 s38, v236, 37
	v_readlane_b32 s39, v236, 38
	v_readlane_b32 s48, v236, 47
	v_readlane_b32 s49, v236, 48
	v_readlane_b32 s50, v236, 49
	v_readlane_b32 s51, v236, 50
	v_readlane_b32 s42, v237, 23
	v_readlane_b32 s43, v237, 24
	v_readlane_b32 s44, v237, 25
	v_readlane_b32 s45, v237, 26
	v_readlane_b32 s46, v237, 27
	v_readlane_b32 s47, v237, 28
	s_addc_u32 s7, s41, s7
	v_lshl_add_u64 v[4:5], s[6:7], 0, v[2:3]
	s_mov_b64 s[6:7], 0x400
	v_readlane_b32 s36, v237, 45
	v_lshl_add_u64 v[42:43], v[4:5], 0, s[6:7]
	s_lshl_b64 s[6:7], s[92:93], 11
	s_lshl_b64 s[8:9], s[96:97], 12
	v_readlane_b32 s48, v237, 57
	v_readlane_b32 s49, v237, 58
	s_add_u32 s8, s48, s8
	v_lshlrev_b32_e32 v2, 3, v78
	s_addc_u32 s9, s49, s9
	v_readlane_b32 s37, v237, 46
	v_readlane_b32 s38, v237, 47
	v_readlane_b32 s39, v237, 48
	v_readlane_b32 s40, v237, 49
	v_readlane_b32 s41, v237, 50
	v_readlane_b32 s42, v237, 51
	v_readlane_b32 s43, v237, 52
	v_readlane_b32 s44, v237, 53
	v_readlane_b32 s45, v237, 54
	v_readlane_b32 s46, v237, 55
	v_readlane_b32 s47, v237, 56
	v_readlane_b32 s50, v237, 59
	v_readlane_b32 s51, v237, 60
	v_lshl_add_u64 v[2:3], s[8:9], 0, v[2:3]
	s_mov_b64 s[8:9], 0x800
	v_readlane_b32 s36, v237, 3
	v_lshl_add_u64 v[44:45], v[2:3], 0, s[8:9]
	v_cndmask_b32_e64 v2, 0, 1, s[0:1]
	v_readlane_b32 s37, v237, 4
	s_lshl_b64 s[8:9], s[92:93], 12
	v_mov_b32_e32 v1, 0x358637bd
	v_cmp_ne_u32_e64 s[0:1], 1, v2
	s_mov_b32 s10, 0xc3e00000
	v_mov_b32_e32 v52, 0x43e00000
	s_mov_b32 s11, s96
	v_readlane_b32 s38, v237, 5
	v_readlane_b32 s39, v237, 6
	v_readlane_b32 s40, v237, 7
	v_readlane_b32 s41, v237, 8
	v_readlane_b32 s42, v237, 9
	v_readlane_b32 s43, v237, 10
	v_readlane_b32 s44, v237, 11
	v_readlane_b32 s45, v237, 12
	v_readlane_b32 s46, v237, 13
	v_readlane_b32 s47, v237, 14
	v_readlane_b32 s48, v237, 15
	v_readlane_b32 s49, v237, 16
	v_readlane_b32 s50, v237, 17
	v_readlane_b32 s51, v237, 18
	global_load_dwordx4 v[80:83], v[30:31], off
	global_load_dwordx4 v[84:87], v[30:31], off offset:1024
	global_load_dwordx4 v[88:91], v[30:31], off offset:2048
	global_load_dwordx4 v[92:95], v[30:31], off offset:3072
	global_load_dwordx4 v[96:99], v[32:33], off
	global_load_dwordx4 v[100:103], v[34:35], off
	global_load_dwordx4 v[104:107], v[36:37], off
	global_load_dwordx4 v[108:111], v[38:39], off
	s_branch .LBB0_176

.LBB0_176:
	global_load_dwordx4 v[48:51], v[40:41], off offset:-4096
	global_load_dwordx4 v[26:29], v[40:41], off offset:-3072
	global_load_dwordx4 v[22:25], v[40:41], off offset:-2048
	global_load_dwordx4 v[18:21], v[40:41], off offset:-1024
	global_load_dwordx4 v[14:17], v[40:41], off
	global_load_dwordx4 v[10:13], v[40:41], off offset:1024
	global_load_dwordx4 v[6:9], v[40:41], off offset:2048
	global_load_dwordx4 v[2:5], v[40:41], off offset:3072
	s_and_b64 vcc, exec, s[0:1]
	s_waitcnt vmcnt(7)
	v_mul_f32_e32 v46, v49, v49
	v_mul_f32_e32 v47, v51, v51
	s_waitcnt vmcnt(6)
	v_mul_f32_e32 v53, v27, v27
	v_mul_f32_e32 v58, v29, v29
	s_waitcnt vmcnt(5)
	v_mul_f32_e32 v59, v23, v23
	v_mul_f32_e32 v60, v25, v25
	v_fmac_f32_e32 v46, v48, v48
	v_fmac_f32_e32 v47, v50, v50
	v_fmac_f32_e32 v53, v26, v26
	v_fmac_f32_e32 v58, v28, v28
	s_waitcnt vmcnt(4)
	v_mul_f32_e32 v61, v19, v19
	v_mul_f32_e32 v62, v21, v21
	v_fmac_f32_e32 v59, v22, v22
	v_fmac_f32_e32 v60, v24, v24
	v_add_f32_e32 v46, v46, v47
	v_add_f32_e32 v47, v53, v58
	s_waitcnt vmcnt(3)
	v_mul_f32_e32 v63, v15, v15
	v_mul_f32_e32 v64, v17, v17
	v_fmac_f32_e32 v61, v18, v18
	v_fmac_f32_e32 v62, v20, v20
	v_add_f32_e32 v53, v59, v60
	v_add_f32_e32 v46, v46, v47
	s_waitcnt vmcnt(2)
	v_mul_f32_e32 v65, v11, v11
	v_mul_f32_e32 v66, v13, v13
	v_fmac_f32_e32 v63, v14, v14
	v_fmac_f32_e32 v64, v16, v16
	v_add_f32_e32 v58, v61, v62
	v_add_f32_e32 v46, v46, v53
	s_waitcnt vmcnt(1)
	v_mul_f32_e32 v67, v7, v7
	v_mul_f32_e32 v68, v9, v9
	v_fmac_f32_e32 v65, v10, v10
	v_fmac_f32_e32 v66, v12, v12
	v_add_f32_e32 v59, v63, v64
	v_add_f32_e32 v46, v46, v58
	s_waitcnt vmcnt(0)
	v_mul_f32_e32 v69, v3, v3
	v_mul_f32_e32 v70, v5, v5
	v_fmac_f32_e32 v67, v6, v6
	v_fmac_f32_e32 v68, v8, v8
	v_add_f32_e32 v60, v65, v66
	v_add_f32_e32 v46, v46, v59
	v_fmac_f32_e32 v69, v2, v2
	v_fmac_f32_e32 v70, v4, v4
	v_add_f32_e32 v61, v67, v68
	v_add_f32_e32 v46, v46, v60
	v_add_f32_e32 v62, v69, v70
	v_add_f32_e32 v46, v46, v61
	v_add_f32_e32 v46, v46, v62
	s_nop 1
	v_add_f32_dpp v46, v46, v46 row_ror:8 row_mask:0xf bank_mask:0xf bound_ctrl:1
	s_nop 1
	v_add_f32_dpp v46, v46, v46 row_ror:4 row_mask:0xf bank_mask:0xf bound_ctrl:1
	s_nop 1
	v_add_f32_dpp v46, v46, v46 row_ror:2 row_mask:0xf bank_mask:0xf bound_ctrl:1
	s_nop 1
	v_add_f32_dpp v46, v46, v46 row_ror:1 row_mask:0xf bank_mask:0xf bound_ctrl:1
	v_mov_b32_e32 v47, v46
	s_nop 1
	v_permlane16_swap_b32_e32 v46, v47
	v_add_f32_e32 v46, v46, v47
	v_mov_b32_e32 v47, v46
	s_nop 1
	v_permlane32_swap_b32_e32 v46, v47
	v_add_f32_e32 v46, v46, v47
	v_fmamk_f32 v46, v46, 0x3a000000, v1
	v_rsq_f32_e32 v46, v46
	s_nop 0
	v_pk_mul_f32 v[58:59], v[48:49], v[46:47] op_sel_hi:[1,0]
	v_pk_mul_f32 v[48:49], v[50:51], v[46:47] op_sel_hi:[1,0]
	v_pk_mul_f32 v[50:51], v[80:81], v[58:59]
	v_pk_mul_f32 v[48:49], v[82:83], v[48:49]
	v_cvt_pk_bf16_f32 v54, v50, v51
	s_nop 0
	v_cvt_pk_bf16_f32 v55, v48, v49
	global_store_dwordx2 v[44:45], v[54:55], off offset:-2048
	s_cbranch_vccnz .LBB0_178
	v_mul_f32_e32 v47, 0x41000000, v50
	v_mul_f32_e32 v50, 0x41000000, v51
	v_med3_f32 v47, v47, s10, v52
	v_med3_f32 v50, v50, s10, v52
	v_mov_b32_e32 v51, 0
	v_cvt_pk_fp8_f32 v51, v47, v50
	v_mul_f32_e32 v48, 0x41000000, v48
	v_mul_f32_e32 v47, 0x41000000, v49
	v_med3_f32 v48, v48, s10, v52
	v_med3_f32 v47, v47, s10, v52
	v_cvt_pk_fp8_f32 v51, v48, v47 op_sel:[0,0,1]
	global_store_dword v[42:43], v51, off offset:-1024
.LBB0_178:
	v_mov_b32_e32 v47, v46
	v_mov_b32_e32 v48, v46
	v_mov_b32_e32 v49, v46
	v_pk_mul_f32 v[28:29], v[28:29], v[48:49]
	v_pk_mul_f32 v[50:51], v[26:27], v[46:47]
	s_and_b64 vcc, exec, s[0:1]
	v_pk_mul_f32 v[26:27], v[28:29], v[86:87]
	v_pk_mul_f32 v[28:29], v[50:51], v[84:85]
	s_nop 0
	v_cvt_pk_bf16_f32 v50, v28, v29
	v_cvt_pk_bf16_f32 v51, v26, v27
	global_store_dwordx2 v[44:45], v[50:51], off offset:-1536
	s_cbranch_vccnz .LBB0_180
	v_mul_f32_e32 v28, 0x41000000, v28
	v_mul_f32_e32 v29, 0x41000000, v29
	v_med3_f32 v28, v28, s10, v52
	v_med3_f32 v29, v29, s10, v52
	v_mov_b32_e32 v50, 0
	v_cvt_pk_fp8_f32 v50, v28, v29
	v_mul_f32_e32 v26, 0x41000000, v26
	v_mul_f32_e32 v27, 0x41000000, v27
	v_med3_f32 v26, v26, s10, v52
	v_med3_f32 v27, v27, s10, v52
	v_cvt_pk_fp8_f32 v50, v26, v27 op_sel:[0,0,1]
	global_store_dword v[42:43], v50, off offset:-768
.LBB0_180:
	v_pk_mul_f32 v[24:25], v[24:25], v[48:49]
	v_pk_mul_f32 v[48:49], v[22:23], v[46:47]
	s_and_b64 vcc, exec, s[0:1]
	v_pk_mul_f32 v[22:23], v[24:25], v[90:91]
	v_pk_mul_f32 v[24:25], v[48:49], v[88:89]
	s_nop 0
	v_cvt_pk_bf16_f32 v26, v24, v25
	v_cvt_pk_bf16_f32 v27, v22, v23
	global_store_dwordx2 v[44:45], v[26:27], off offset:-1024
	s_cbranch_vccnz .LBB0_182
	v_mul_f32_e32 v24, 0x41000000, v24
	v_mul_f32_e32 v25, 0x41000000, v25
	v_med3_f32 v24, v24, s10, v52
	v_med3_f32 v25, v25, s10, v52
	v_mov_b32_e32 v26, 0
	v_cvt_pk_fp8_f32 v26, v24, v25
	v_mul_f32_e32 v22, 0x41000000, v22
	v_mul_f32_e32 v23, 0x41000000, v23
	v_med3_f32 v22, v22, s10, v52
	v_med3_f32 v23, v23, s10, v52
	v_cvt_pk_fp8_f32 v26, v22, v23 op_sel:[0,0,1]
	global_store_dword v[42:43], v26, off offset:-512
.LBB0_182:
	v_mov_b32_e32 v22, v46
	v_mov_b32_e32 v23, v46
	v_pk_mul_f32 v[28:29], v[18:19], v[46:47]
	v_pk_mul_f32 v[18:19], v[20:21], v[22:23]
	s_and_b64 vcc, exec, s[0:1]
	v_pk_mul_f32 v[18:19], v[18:19], v[94:95]
	v_pk_mul_f32 v[20:21], v[28:29], v[92:93]
	s_nop 0
	v_cvt_pk_bf16_f32 v24, v20, v21
	v_cvt_pk_bf16_f32 v25, v18, v19
	global_store_dwordx2 v[44:45], v[24:25], off offset:-512
	s_cbranch_vccnz .LBB0_184
	v_mul_f32_e32 v20, 0x41000000, v20
	v_mul_f32_e32 v21, 0x41000000, v21
	v_med3_f32 v20, v20, s10, v52
	v_med3_f32 v21, v21, s10, v52
	v_mov_b32_e32 v24, 0
	v_cvt_pk_fp8_f32 v24, v20, v21
	v_mul_f32_e32 v18, 0x41000000, v18
	v_mul_f32_e32 v19, 0x41000000, v19
	v_med3_f32 v18, v18, s10, v52
	v_med3_f32 v19, v19, s10, v52
	v_cvt_pk_fp8_f32 v24, v18, v19 op_sel:[0,0,1]
	global_store_dword v[42:43], v24, off offset:-256
.LBB0_184:
	v_pk_mul_f32 v[16:17], v[16:17], v[22:23]
	v_pk_mul_f32 v[22:23], v[14:15], v[46:47]
	s_and_b64 vcc, exec, s[0:1]
	v_pk_mul_f32 v[14:15], v[16:17], v[98:99]
	v_pk_mul_f32 v[16:17], v[22:23], v[96:97]
	s_nop 0
	v_cvt_pk_bf16_f32 v18, v16, v17
	v_cvt_pk_bf16_f32 v19, v14, v15
	global_store_dwordx2 v[44:45], v[18:19], off
	s_cbranch_vccnz .LBB0_186
	v_mul_f32_e32 v16, 0x41000000, v16
	v_mul_f32_e32 v17, 0x41000000, v17
	v_med3_f32 v16, v16, s10, v52
	v_med3_f32 v17, v17, s10, v52
	v_mov_b32_e32 v18, 0
	v_cvt_pk_fp8_f32 v18, v16, v17
	v_mul_f32_e32 v14, 0x41000000, v14
	v_mul_f32_e32 v15, 0x41000000, v15
	v_med3_f32 v14, v14, s10, v52
	v_med3_f32 v15, v15, s10, v52
	v_cvt_pk_fp8_f32 v18, v14, v15 op_sel:[0,0,1]
	global_store_dword v[42:43], v18, off
.LBB0_186:
	v_mov_b32_e32 v14, v46
	v_mov_b32_e32 v15, v46
	v_pk_mul_f32 v[20:21], v[10:11], v[46:47]
	v_pk_mul_f32 v[10:11], v[12:13], v[14:15]
	s_and_b64 vcc, exec, s[0:1]
	v_pk_mul_f32 v[10:11], v[10:11], v[102:103]
	v_pk_mul_f32 v[12:13], v[20:21], v[100:101]
	s_nop 0
	v_cvt_pk_bf16_f32 v16, v12, v13
	v_cvt_pk_bf16_f32 v17, v10, v11
	global_store_dwordx2 v[44:45], v[16:17], off offset:512
	s_cbranch_vccnz .LBB0_188
	v_mul_f32_e32 v12, 0x41000000, v12
	v_mul_f32_e32 v13, 0x41000000, v13
	v_med3_f32 v12, v12, s10, v52
	v_med3_f32 v13, v13, s10, v52
	v_mov_b32_e32 v16, 0
	v_cvt_pk_fp8_f32 v16, v12, v13
	v_mul_f32_e32 v10, 0x41000000, v10
	v_mul_f32_e32 v11, 0x41000000, v11
	v_med3_f32 v10, v10, s10, v52
	v_med3_f32 v11, v11, s10, v52
	v_cvt_pk_fp8_f32 v16, v10, v11 op_sel:[0,0,1]
	global_store_dword v[42:43], v16, off offset:256
.LBB0_188:
	v_pk_mul_f32 v[8:9], v[8:9], v[14:15]
	v_pk_mul_f32 v[14:15], v[6:7], v[46:47]
	s_and_b64 vcc, exec, s[0:1]
	v_pk_mul_f32 v[6:7], v[8:9], v[106:107]
	v_pk_mul_f32 v[8:9], v[14:15], v[104:105]
	s_nop 0
	v_cvt_pk_bf16_f32 v10, v8, v9
	v_cvt_pk_bf16_f32 v11, v6, v7
	global_store_dwordx2 v[44:45], v[10:11], off offset:1024
	s_cbranch_vccnz .LBB0_190
	v_mul_f32_e32 v8, 0x41000000, v8
	v_mul_f32_e32 v9, 0x41000000, v9
	v_med3_f32 v8, v8, s10, v52
	v_med3_f32 v9, v9, s10, v52
	v_mov_b32_e32 v10, 0
	v_cvt_pk_fp8_f32 v10, v8, v9
	v_mul_f32_e32 v6, 0x41000000, v6
	v_mul_f32_e32 v7, 0x41000000, v7
	v_med3_f32 v6, v6, s10, v52
	v_med3_f32 v7, v7, s10, v52
	v_cvt_pk_fp8_f32 v10, v6, v7 op_sel:[0,0,1]
	global_store_dword v[42:43], v10, off offset:512
.LBB0_190:
	v_mov_b32_e32 v10, v46
	v_mov_b32_e32 v11, v46
	v_pk_mul_f32 v[12:13], v[2:3], v[46:47]
	v_pk_mul_f32 v[2:3], v[4:5], v[10:11]
	s_and_b64 vcc, exec, s[0:1]
	v_pk_mul_f32 v[2:3], v[2:3], v[110:111]
	v_pk_mul_f32 v[4:5], v[12:13], v[108:109]
	s_nop 0
	v_cvt_pk_bf16_f32 v6, v4, v5
	v_cvt_pk_bf16_f32 v7, v2, v3
	global_store_dwordx2 v[44:45], v[6:7], off offset:1536
	s_cbranch_vccnz .LBB0_175
	v_mul_f32_e32 v4, 0x41000000, v4
	v_mul_f32_e32 v5, 0x41000000, v5
	v_med3_f32 v4, v4, s10, v52
	v_med3_f32 v5, v5, s10, v52
	v_mov_b32_e32 v6, 0
	v_cvt_pk_fp8_f32 v6, v4, v5
	v_mul_f32_e32 v2, 0x41000000, v2
	v_mul_f32_e32 v3, 0x41000000, v3
	v_med3_f32 v2, v2, s10, v52
	v_med3_f32 v3, v3, s10, v52
	v_cvt_pk_fp8_f32 v6, v2, v3 op_sel:[0,0,1]
	global_store_dword v[42:43], v6, off offset:768
	s_branch .LBB0_175
